# gated short conv (split phase part 2) rewritten by hand: all row loads of a 512-column piece in flight together
# speedup vs baseline: 1.0056x; 1.0056x over previous
.LBB0_371:
	v_readfirstlane_b32 s16, v0
	s_lshr_b32 s16, s16, 6
	s_lshl_b32 s17, s2, 3
	s_add_u32 s16, s16, s17
	s_lshl_b32 s17, s82, 3
	s_add_u32 s18, s96, s17
	s_sub_u32 s18, s18, 1
	v_cvt_f32_u32_e32 v116, s17
	v_cvt_f32_u32_e32 v117, s18
	v_rcp_iflag_f32_e32 v116, v116
	s_nop 0
	v_mul_f32_e32 v116, v117, v116
	v_cvt_u32_f32_e32 v116, v116
	s_nop 0
	v_readfirstlane_b32 s19, v116
	s_mul_i32 s12, s19, s17
	s_cmp_gt_u32 s12, s18
	s_cselect_b32 s13, 1, 0
	s_sub_u32 s19, s19, s13
	s_add_u32 s12, s19, 1
	s_mul_i32 s12, s12, s17
	s_cmp_le_u32 s12, s18
	s_cselect_b32 s13, 1, 0
	s_add_u32 s19, s19, s13
	s_mul_i32 s12, s16, s19
	s_cmp_ge_u32 s12, s96
	s_cbranch_scc1 .Lcv_end
	s_add_u32 s13, s12, s19
	s_min_u32 s13, s13, s96
	v_readlane_b32 s10, v252, 4
	v_readlane_b32 s11, v252, 5
	v_readlane_b32 s14, v255, 34
	s_sub_u32 s10, s10, 0x18
	s_subb_u32 s11, s11, 0
	s_load_dwordx2 s[10:11], s[10:11], 0x0
	v_readlane_b32 s44, v252, 30
	v_readlane_b32 s45, v252, 31
	s_mul_i32 s16, s14, 0x6000
	v_and_b32_e32 v3, 63, v0
	v_lshlrev_b32_e32 v142, 3, v3
	s_mov_b32 s15, 0x3b800000
	s_waitcnt lgkmcnt(0)
	s_add_u32 s38, s10, 0x2a000000
	s_addc_u32 s39, s11, 0
	s_add_u32 s38, s38, 0x1400
	s_addc_u32 s39, s39, 0
	s_add_u32 s40, s10, 0x21800800
	s_addc_u32 s41, s11, 0
	s_add_u32 s44, s44, s16
	s_addc_u32 s45, s45, 0
	s_add_u32 s46, s44, 0x2000
	s_addc_u32 s47, s45, 0
	s_add_u32 s48, s44, 0x4000
	s_addc_u32 s49, s45, 0
	s_sub_u32 s43, s96, 1
.Lcv_chunk:
	s_mov_b32 s42, 0
.Lcv_piece:
	s_lshl_b32 s16, s42, 9
	v_add_u32_e32 v140, s16, v142
	v_lshlrev_b32_e32 v141, 2, v140
	global_load_dwordx4 v[6:9], v141, s[44:45]
	global_load_dwordx4 v[10:13], v141, s[44:45] offset:16
	global_load_dwordx4 v[14:17], v141, s[46:47]
	global_load_dwordx4 v[18:21], v141, s[46:47] offset:16
	global_load_dwordx4 v[22:25], v141, s[48:49]
	global_load_dwordx4 v[26:29], v141, s[48:49] offset:16
	s_max_u32 s16, s12, 1
	s_sub_u32 s16, s16, 1
	s_mul_i32 s17, s16, 0x3400
	s_add_u32 s52, s38, s17
	s_addc_u32 s53, s39, 0
	global_load_dwordx2 v[30:31], v140, s[52:53] offset:-2048 nt
	global_load_dwordx2 v[52:53], v140, s[52:53] offset:2048 nt
	s_add_u32 s16, s12, 0
	s_min_u32 s16, s16, s43
	s_mul_i32 s17, s16, 0x3400
	s_add_u32 s52, s38, s17
	s_addc_u32 s53, s39, 0
	global_load_dwordx2 v[32:33], v140, s[52:53] offset:-2048 nt
	global_load_dwordx2 v[54:55], v140, s[52:53] offset:2048 nt
	global_load_dwordx2 v[74:75], v140, s[52:53] nt
	s_add_u32 s16, s12, 1
	s_min_u32 s16, s16, s43
	s_mul_i32 s17, s16, 0x3400
	s_add_u32 s52, s38, s17
	s_addc_u32 s53, s39, 0
	global_load_dwordx2 v[34:35], v140, s[52:53] offset:-2048 nt
	global_load_dwordx2 v[56:57], v140, s[52:53] offset:2048 nt
	global_load_dwordx2 v[76:77], v140, s[52:53] nt
	s_add_u32 s16, s12, 2
	s_min_u32 s16, s16, s43
	s_mul_i32 s17, s16, 0x3400
	s_add_u32 s52, s38, s17
	s_addc_u32 s53, s39, 0
	global_load_dwordx2 v[36:37], v140, s[52:53] offset:-2048 nt
	global_load_dwordx2 v[58:59], v140, s[52:53] offset:2048 nt
	global_load_dwordx2 v[78:79], v140, s[52:53] nt
	s_add_u32 s16, s12, 3
	s_min_u32 s16, s16, s43
	s_mul_i32 s17, s16, 0x3400
	s_add_u32 s52, s38, s17
	s_addc_u32 s53, s39, 0
	global_load_dwordx2 v[38:39], v140, s[52:53] offset:-2048 nt
	global_load_dwordx2 v[60:61], v140, s[52:53] offset:2048 nt
	global_load_dwordx2 v[80:81], v140, s[52:53] nt
	s_add_u32 s16, s12, 4
	s_min_u32 s16, s16, s43
	s_mul_i32 s17, s16, 0x3400
	s_add_u32 s52, s38, s17
	s_addc_u32 s53, s39, 0
	global_load_dwordx2 v[40:41], v140, s[52:53] offset:-2048 nt
	global_load_dwordx2 v[62:63], v140, s[52:53] offset:2048 nt
	global_load_dwordx2 v[82:83], v140, s[52:53] nt
	s_add_u32 s16, s12, 5
	s_min_u32 s16, s16, s43
	s_mul_i32 s17, s16, 0x3400
	s_add_u32 s52, s38, s17
	s_addc_u32 s53, s39, 0
	global_load_dwordx2 v[42:43], v140, s[52:53] offset:-2048 nt
	global_load_dwordx2 v[64:65], v140, s[52:53] offset:2048 nt
	global_load_dwordx2 v[84:85], v140, s[52:53] nt
	s_add_u32 s16, s12, 6
	s_min_u32 s16, s16, s43
	s_mul_i32 s17, s16, 0x3400
	s_add_u32 s52, s38, s17
	s_addc_u32 s53, s39, 0
	global_load_dwordx2 v[44:45], v140, s[52:53] offset:-2048 nt
	global_load_dwordx2 v[66:67], v140, s[52:53] offset:2048 nt
	global_load_dwordx2 v[86:87], v140, s[52:53] nt
	s_add_u32 s16, s12, 7
	s_min_u32 s16, s16, s43
	s_mul_i32 s17, s16, 0x3400
	s_add_u32 s52, s38, s17
	s_addc_u32 s53, s39, 0
	global_load_dwordx2 v[46:47], v140, s[52:53] offset:-2048 nt
	global_load_dwordx2 v[68:69], v140, s[52:53] offset:2048 nt
	global_load_dwordx2 v[88:89], v140, s[52:53] nt
	s_add_u32 s16, s12, 8
	s_min_u32 s16, s16, s43
	s_mul_i32 s17, s16, 0x3400
	s_add_u32 s52, s38, s17
	s_addc_u32 s53, s39, 0
	global_load_dwordx2 v[48:49], v140, s[52:53] offset:-2048 nt
	global_load_dwordx2 v[70:71], v140, s[52:53] offset:2048 nt
	global_load_dwordx2 v[90:91], v140, s[52:53] nt
	s_add_u32 s16, s12, 9
	s_min_u32 s16, s16, s43
	s_mul_i32 s17, s16, 0x3400
	s_add_u32 s52, s38, s17
	s_addc_u32 s53, s39, 0
	global_load_dwordx2 v[50:51], v140, s[52:53] offset:-2048 nt
	global_load_dwordx2 v[72:73], v140, s[52:53] offset:2048 nt
	s_waitcnt vmcnt(31)
	v_mul_f32_e32 v6, s15, v6
	v_mul_f32_e32 v7, s15, v7
	v_mul_f32_e32 v8, s15, v8
	v_mul_f32_e32 v9, s15, v9
	v_mul_f32_e32 v10, s15, v10
	v_mul_f32_e32 v11, s15, v11
	v_mul_f32_e32 v12, s15, v12
	v_mul_f32_e32 v13, s15, v13
	v_mul_f32_e32 v14, s15, v14
	v_mul_f32_e32 v15, s15, v15
	v_mul_f32_e32 v16, s15, v16
	v_mul_f32_e32 v17, s15, v17
	v_mul_f32_e32 v18, s15, v18
	v_mul_f32_e32 v19, s15, v19
	v_mul_f32_e32 v20, s15, v20
	v_mul_f32_e32 v21, s15, v21
	v_mul_f32_e32 v22, s15, v22
	v_mul_f32_e32 v23, s15, v23
	v_mul_f32_e32 v24, s15, v24
	v_mul_f32_e32 v25, s15, v25
	v_mul_f32_e32 v26, s15, v26
	v_mul_f32_e32 v27, s15, v27
	v_mul_f32_e32 v28, s15, v28
	v_mul_f32_e32 v29, s15, v29
	s_waitcnt vmcnt(0)
	v_cvt_pk_f32_fp8_e32 v[116:117], v30
	v_cvt_pk_f32_fp8_sdwa v[118:119], v30 src0_sel:WORD_1
	v_cvt_pk_f32_fp8_e32 v[120:121], v31
	v_cvt_pk_f32_fp8_sdwa v[122:123], v31 src0_sel:WORD_1
	v_cvt_pk_f32_fp8_e32 v[124:125], v52
	v_cvt_pk_f32_fp8_sdwa v[126:127], v52 src0_sel:WORD_1
	v_cvt_pk_f32_fp8_e32 v[128:129], v53
	v_cvt_pk_f32_fp8_sdwa v[130:131], v53 src0_sel:WORD_1
	v_pk_mul_f32 v[92:93], v[116:117], v[124:125]
	v_pk_mul_f32 v[94:95], v[118:119], v[126:127]
	v_pk_mul_f32 v[96:97], v[120:121], v[128:129]
	v_pk_mul_f32 v[98:99], v[122:123], v[130:131]
	v_cvt_pk_f32_fp8_e32 v[116:117], v32
	v_cvt_pk_f32_fp8_sdwa v[118:119], v32 src0_sel:WORD_1
	v_cvt_pk_f32_fp8_e32 v[120:121], v33
	v_cvt_pk_f32_fp8_sdwa v[122:123], v33 src0_sel:WORD_1
	v_cvt_pk_f32_fp8_e32 v[124:125], v54
	v_cvt_pk_f32_fp8_sdwa v[126:127], v54 src0_sel:WORD_1
	v_cvt_pk_f32_fp8_e32 v[128:129], v55
	v_cvt_pk_f32_fp8_sdwa v[130:131], v55 src0_sel:WORD_1
	v_pk_mul_f32 v[100:101], v[116:117], v[124:125]
	v_pk_mul_f32 v[102:103], v[118:119], v[126:127]
	v_pk_mul_f32 v[104:105], v[120:121], v[128:129]
	v_pk_mul_f32 v[106:107], v[122:123], v[130:131]
	v_cvt_pk_f32_fp8_e32 v[116:117], v34
	v_cvt_pk_f32_fp8_sdwa v[118:119], v34 src0_sel:WORD_1
	v_cvt_pk_f32_fp8_e32 v[120:121], v35
	v_cvt_pk_f32_fp8_sdwa v[122:123], v35 src0_sel:WORD_1
	v_cvt_pk_f32_fp8_e32 v[124:125], v56
	v_cvt_pk_f32_fp8_sdwa v[126:127], v56 src0_sel:WORD_1
	v_cvt_pk_f32_fp8_e32 v[128:129], v57
	v_cvt_pk_f32_fp8_sdwa v[130:131], v57 src0_sel:WORD_1
	v_pk_mul_f32 v[108:109], v[116:117], v[124:125]
	v_pk_mul_f32 v[110:111], v[118:119], v[126:127]
	v_pk_mul_f32 v[112:113], v[120:121], v[128:129]
	v_pk_mul_f32 v[114:115], v[122:123], v[130:131]
	s_add_u32 s16, s12, 0
	s_cmp_ge_u32 s16, s13
	s_cbranch_scc1 .Lcv_piece_done
	s_movk_i32 s17, 0xff
	s_cmp_lt_u32 s16, 0x4000
	s_cselect_b32 s17, 0xfff, s17
	s_and_b32 s18, s16, s17
	s_cmp_eq_u32 s18, 0
	s_cbranch_scc1 .Lcv_nohp_0
	v_pk_mul_f32 v[132:133], v[6:7], v[92:93]
	v_pk_mul_f32 v[134:135], v[8:9], v[94:95]
	v_pk_mul_f32 v[136:137], v[10:11], v[96:97]
	v_pk_mul_f32 v[138:139], v[12:13], v[98:99]
	s_branch .Lcv_hp_0
.Lcv_nohp_0:
	v_mov_b32_e32 v132, 0
	v_mov_b32_e32 v133, 0
	v_mov_b32_e32 v134, 0
	v_mov_b32_e32 v135, 0
	v_mov_b32_e32 v136, 0
	v_mov_b32_e32 v137, 0
	v_mov_b32_e32 v138, 0
	v_mov_b32_e32 v139, 0
.Lcv_hp_0:
	v_pk_fma_f32 v[132:133], v[14:15], v[100:101], v[132:133]
	v_pk_fma_f32 v[134:135], v[16:17], v[102:103], v[134:135]
	v_pk_fma_f32 v[136:137], v[18:19], v[104:105], v[136:137]
	v_pk_fma_f32 v[138:139], v[20:21], v[106:107], v[138:139]
	s_cmp_eq_u32 s18, s17
	s_cbranch_scc1 .Lcv_nohn_0
	v_pk_fma_f32 v[132:133], v[22:23], v[108:109], v[132:133]
	v_pk_fma_f32 v[134:135], v[24:25], v[110:111], v[134:135]
	v_pk_fma_f32 v[136:137], v[26:27], v[112:113], v[136:137]
	v_pk_fma_f32 v[138:139], v[28:29], v[114:115], v[138:139]
.Lcv_nohn_0:
	v_cvt_pk_f32_fp8_e32 v[116:117], v74
	v_cvt_pk_f32_fp8_sdwa v[118:119], v74 src0_sel:WORD_1
	v_cvt_pk_f32_fp8_e32 v[120:121], v75
	v_cvt_pk_f32_fp8_sdwa v[122:123], v75 src0_sel:WORD_1
	v_pk_mul_f32 v[116:117], v[116:117], 0.5 op_sel_hi:[1,0]
	v_pk_mul_f32 v[118:119], v[118:119], 0.5 op_sel_hi:[1,0]
	v_pk_mul_f32 v[120:121], v[120:121], 0.5 op_sel_hi:[1,0]
	v_pk_mul_f32 v[122:123], v[122:123], 0.5 op_sel_hi:[1,0]
	v_pk_mul_f32 v[132:133], v[116:117], v[132:133]
	v_pk_mul_f32 v[134:135], v[118:119], v[134:135]
	v_pk_mul_f32 v[136:137], v[120:121], v[136:137]
	v_pk_mul_f32 v[138:139], v[122:123], v[138:139]
	v_med3_f32 v132, v132, s79, v204
	v_med3_f32 v133, v133, s79, v204
	v_med3_f32 v134, v134, s79, v204
	v_med3_f32 v135, v135, s79, v204
	v_med3_f32 v136, v136, s79, v204
	v_med3_f32 v137, v137, s79, v204
	v_med3_f32 v138, v138, s79, v204
	v_med3_f32 v139, v139, s79, v204
	v_mov_b32_e32 v124, 0
	v_mov_b32_e32 v125, 0
	v_cvt_pk_fp8_f32 v124, v132, v133
	v_cvt_pk_fp8_f32 v125, v136, v137
	v_cvt_pk_fp8_f32 v124, v134, v135 op_sel:[0,0,1]
	v_cvt_pk_fp8_f32 v125, v138, v139 op_sel:[0,0,1]
	s_lshl_b32 s17, s16, 12
	s_add_u32 s52, s40, s17
	s_addc_u32 s53, s41, 0
	global_store_dwordx2 v140, v[124:125], s[52:53]
	v_cvt_pk_f32_fp8_e32 v[116:117], v36
	v_cvt_pk_f32_fp8_sdwa v[118:119], v36 src0_sel:WORD_1
	v_cvt_pk_f32_fp8_e32 v[120:121], v37
	v_cvt_pk_f32_fp8_sdwa v[122:123], v37 src0_sel:WORD_1
	v_cvt_pk_f32_fp8_e32 v[124:125], v58
	v_cvt_pk_f32_fp8_sdwa v[126:127], v58 src0_sel:WORD_1
	v_cvt_pk_f32_fp8_e32 v[128:129], v59
	v_cvt_pk_f32_fp8_sdwa v[130:131], v59 src0_sel:WORD_1
	v_pk_mul_f32 v[92:93], v[116:117], v[124:125]
	v_pk_mul_f32 v[94:95], v[118:119], v[126:127]
	v_pk_mul_f32 v[96:97], v[120:121], v[128:129]
	v_pk_mul_f32 v[98:99], v[122:123], v[130:131]
	s_add_u32 s16, s12, 1
	s_cmp_ge_u32 s16, s13
	s_cbranch_scc1 .Lcv_piece_done
	s_movk_i32 s17, 0xff
	s_cmp_lt_u32 s16, 0x4000
	s_cselect_b32 s17, 0xfff, s17
	s_and_b32 s18, s16, s17
	s_cmp_eq_u32 s18, 0
	s_cbranch_scc1 .Lcv_nohp_1
	v_pk_mul_f32 v[132:133], v[6:7], v[100:101]
	v_pk_mul_f32 v[134:135], v[8:9], v[102:103]
	v_pk_mul_f32 v[136:137], v[10:11], v[104:105]
	v_pk_mul_f32 v[138:139], v[12:13], v[106:107]
	s_branch .Lcv_hp_1

.Lcv_hp_1:
	v_pk_fma_f32 v[132:133], v[14:15], v[108:109], v[132:133]
	v_pk_fma_f32 v[134:135], v[16:17], v[110:111], v[134:135]
	v_pk_fma_f32 v[136:137], v[18:19], v[112:113], v[136:137]
	v_pk_fma_f32 v[138:139], v[20:21], v[114:115], v[138:139]
	s_cmp_eq_u32 s18, s17
	s_cbranch_scc1 .Lcv_nohn_1
	v_pk_fma_f32 v[132:133], v[22:23], v[92:93], v[132:133]
	v_pk_fma_f32 v[134:135], v[24:25], v[94:95], v[134:135]
	v_pk_fma_f32 v[136:137], v[26:27], v[96:97], v[136:137]
	v_pk_fma_f32 v[138:139], v[28:29], v[98:99], v[138:139]
.Lcv_nohn_1:
	v_cvt_pk_f32_fp8_e32 v[116:117], v76
	v_cvt_pk_f32_fp8_sdwa v[118:119], v76 src0_sel:WORD_1
	v_cvt_pk_f32_fp8_e32 v[120:121], v77
	v_cvt_pk_f32_fp8_sdwa v[122:123], v77 src0_sel:WORD_1
	v_pk_mul_f32 v[116:117], v[116:117], 0.5 op_sel_hi:[1,0]
	v_pk_mul_f32 v[118:119], v[118:119], 0.5 op_sel_hi:[1,0]
	v_pk_mul_f32 v[120:121], v[120:121], 0.5 op_sel_hi:[1,0]
	v_pk_mul_f32 v[122:123], v[122:123], 0.5 op_sel_hi:[1,0]
	v_pk_mul_f32 v[132:133], v[116:117], v[132:133]
	v_pk_mul_f32 v[134:135], v[118:119], v[134:135]
	v_pk_mul_f32 v[136:137], v[120:121], v[136:137]
	v_pk_mul_f32 v[138:139], v[122:123], v[138:139]
	v_med3_f32 v132, v132, s79, v204
	v_med3_f32 v133, v133, s79, v204
	v_med3_f32 v134, v134, s79, v204
	v_med3_f32 v135, v135, s79, v204
	v_med3_f32 v136, v136, s79, v204
	v_med3_f32 v137, v137, s79, v204
	v_med3_f32 v138, v138, s79, v204
	v_med3_f32 v139, v139, s79, v204
	v_mov_b32_e32 v124, 0
	v_mov_b32_e32 v125, 0
	v_cvt_pk_fp8_f32 v124, v132, v133
	v_cvt_pk_fp8_f32 v125, v136, v137
	v_cvt_pk_fp8_f32 v124, v134, v135 op_sel:[0,0,1]
	v_cvt_pk_fp8_f32 v125, v138, v139 op_sel:[0,0,1]
	s_lshl_b32 s17, s16, 12
	s_add_u32 s52, s40, s17
	s_addc_u32 s53, s41, 0
	global_store_dwordx2 v140, v[124:125], s[52:53]
	v_cvt_pk_f32_fp8_e32 v[116:117], v38
	v_cvt_pk_f32_fp8_sdwa v[118:119], v38 src0_sel:WORD_1
	v_cvt_pk_f32_fp8_e32 v[120:121], v39
	v_cvt_pk_f32_fp8_sdwa v[122:123], v39 src0_sel:WORD_1
	v_cvt_pk_f32_fp8_e32 v[124:125], v60
	v_cvt_pk_f32_fp8_sdwa v[126:127], v60 src0_sel:WORD_1
	v_cvt_pk_f32_fp8_e32 v[128:129], v61
	v_cvt_pk_f32_fp8_sdwa v[130:131], v61 src0_sel:WORD_1
	v_pk_mul_f32 v[100:101], v[116:117], v[124:125]
	v_pk_mul_f32 v[102:103], v[118:119], v[126:127]
	v_pk_mul_f32 v[104:105], v[120:121], v[128:129]
	v_pk_mul_f32 v[106:107], v[122:123], v[130:131]
	s_add_u32 s16, s12, 2
	s_cmp_ge_u32 s16, s13
	s_cbranch_scc1 .Lcv_piece_done
	s_movk_i32 s17, 0xff
	s_cmp_lt_u32 s16, 0x4000
	s_cselect_b32 s17, 0xfff, s17
	s_and_b32 s18, s16, s17
	s_cmp_eq_u32 s18, 0
	s_cbranch_scc1 .Lcv_nohp_2
	v_pk_mul_f32 v[132:133], v[6:7], v[108:109]
	v_pk_mul_f32 v[134:135], v[8:9], v[110:111]
	v_pk_mul_f32 v[136:137], v[10:11], v[112:113]
	v_pk_mul_f32 v[138:139], v[12:13], v[114:115]
	s_branch .Lcv_hp_2

.Lcv_hp_2:
	v_pk_fma_f32 v[132:133], v[14:15], v[92:93], v[132:133]
	v_pk_fma_f32 v[134:135], v[16:17], v[94:95], v[134:135]
	v_pk_fma_f32 v[136:137], v[18:19], v[96:97], v[136:137]
	v_pk_fma_f32 v[138:139], v[20:21], v[98:99], v[138:139]
	s_cmp_eq_u32 s18, s17
	s_cbranch_scc1 .Lcv_nohn_2
	v_pk_fma_f32 v[132:133], v[22:23], v[100:101], v[132:133]
	v_pk_fma_f32 v[134:135], v[24:25], v[102:103], v[134:135]
	v_pk_fma_f32 v[136:137], v[26:27], v[104:105], v[136:137]
	v_pk_fma_f32 v[138:139], v[28:29], v[106:107], v[138:139]
.Lcv_nohn_2:
	v_cvt_pk_f32_fp8_e32 v[116:117], v78
	v_cvt_pk_f32_fp8_sdwa v[118:119], v78 src0_sel:WORD_1
	v_cvt_pk_f32_fp8_e32 v[120:121], v79
	v_cvt_pk_f32_fp8_sdwa v[122:123], v79 src0_sel:WORD_1
	v_pk_mul_f32 v[116:117], v[116:117], 0.5 op_sel_hi:[1,0]
	v_pk_mul_f32 v[118:119], v[118:119], 0.5 op_sel_hi:[1,0]
	v_pk_mul_f32 v[120:121], v[120:121], 0.5 op_sel_hi:[1,0]
	v_pk_mul_f32 v[122:123], v[122:123], 0.5 op_sel_hi:[1,0]
	v_pk_mul_f32 v[132:133], v[116:117], v[132:133]
	v_pk_mul_f32 v[134:135], v[118:119], v[134:135]
	v_pk_mul_f32 v[136:137], v[120:121], v[136:137]
	v_pk_mul_f32 v[138:139], v[122:123], v[138:139]
	v_med3_f32 v132, v132, s79, v204
	v_med3_f32 v133, v133, s79, v204
	v_med3_f32 v134, v134, s79, v204
	v_med3_f32 v135, v135, s79, v204
	v_med3_f32 v136, v136, s79, v204
	v_med3_f32 v137, v137, s79, v204
	v_med3_f32 v138, v138, s79, v204
	v_med3_f32 v139, v139, s79, v204
	v_mov_b32_e32 v124, 0
	v_mov_b32_e32 v125, 0
	v_cvt_pk_fp8_f32 v124, v132, v133
	v_cvt_pk_fp8_f32 v125, v136, v137
	v_cvt_pk_fp8_f32 v124, v134, v135 op_sel:[0,0,1]
	v_cvt_pk_fp8_f32 v125, v138, v139 op_sel:[0,0,1]
	s_lshl_b32 s17, s16, 12
	s_add_u32 s52, s40, s17
	s_addc_u32 s53, s41, 0
	global_store_dwordx2 v140, v[124:125], s[52:53]
	v_cvt_pk_f32_fp8_e32 v[116:117], v40
	v_cvt_pk_f32_fp8_sdwa v[118:119], v40 src0_sel:WORD_1
	v_cvt_pk_f32_fp8_e32 v[120:121], v41
	v_cvt_pk_f32_fp8_sdwa v[122:123], v41 src0_sel:WORD_1
	v_cvt_pk_f32_fp8_e32 v[124:125], v62
	v_cvt_pk_f32_fp8_sdwa v[126:127], v62 src0_sel:WORD_1
	v_cvt_pk_f32_fp8_e32 v[128:129], v63
	v_cvt_pk_f32_fp8_sdwa v[130:131], v63 src0_sel:WORD_1
	v_pk_mul_f32 v[108:109], v[116:117], v[124:125]
	v_pk_mul_f32 v[110:111], v[118:119], v[126:127]
	v_pk_mul_f32 v[112:113], v[120:121], v[128:129]
	v_pk_mul_f32 v[114:115], v[122:123], v[130:131]
	s_add_u32 s16, s12, 3
	s_cmp_ge_u32 s16, s13
	s_cbranch_scc1 .Lcv_piece_done
	s_movk_i32 s17, 0xff
	s_cmp_lt_u32 s16, 0x4000
	s_cselect_b32 s17, 0xfff, s17
	s_and_b32 s18, s16, s17
	s_cmp_eq_u32 s18, 0
	s_cbranch_scc1 .Lcv_nohp_3
	v_pk_mul_f32 v[132:133], v[6:7], v[92:93]
	v_pk_mul_f32 v[134:135], v[8:9], v[94:95]
	v_pk_mul_f32 v[136:137], v[10:11], v[96:97]
	v_pk_mul_f32 v[138:139], v[12:13], v[98:99]
	s_branch .Lcv_hp_3

.Lcv_nohn_3:
	v_cvt_pk_f32_fp8_e32 v[116:117], v80
	v_cvt_pk_f32_fp8_sdwa v[118:119], v80 src0_sel:WORD_1
	v_cvt_pk_f32_fp8_e32 v[120:121], v81
	v_cvt_pk_f32_fp8_sdwa v[122:123], v81 src0_sel:WORD_1
	v_pk_mul_f32 v[116:117], v[116:117], 0.5 op_sel_hi:[1,0]
	v_pk_mul_f32 v[118:119], v[118:119], 0.5 op_sel_hi:[1,0]
	v_pk_mul_f32 v[120:121], v[120:121], 0.5 op_sel_hi:[1,0]
	v_pk_mul_f32 v[122:123], v[122:123], 0.5 op_sel_hi:[1,0]
	v_pk_mul_f32 v[132:133], v[116:117], v[132:133]
	v_pk_mul_f32 v[134:135], v[118:119], v[134:135]
	v_pk_mul_f32 v[136:137], v[120:121], v[136:137]
	v_pk_mul_f32 v[138:139], v[122:123], v[138:139]
	v_med3_f32 v132, v132, s79, v204
	v_med3_f32 v133, v133, s79, v204
	v_med3_f32 v134, v134, s79, v204
	v_med3_f32 v135, v135, s79, v204
	v_med3_f32 v136, v136, s79, v204
	v_med3_f32 v137, v137, s79, v204
	v_med3_f32 v138, v138, s79, v204
	v_med3_f32 v139, v139, s79, v204
	v_mov_b32_e32 v124, 0
	v_mov_b32_e32 v125, 0
	v_cvt_pk_fp8_f32 v124, v132, v133
	v_cvt_pk_fp8_f32 v125, v136, v137
	v_cvt_pk_fp8_f32 v124, v134, v135 op_sel:[0,0,1]
	v_cvt_pk_fp8_f32 v125, v138, v139 op_sel:[0,0,1]
	s_lshl_b32 s17, s16, 12
	s_add_u32 s52, s40, s17
	s_addc_u32 s53, s41, 0
	global_store_dwordx2 v140, v[124:125], s[52:53]
	v_cvt_pk_f32_fp8_e32 v[116:117], v42
	v_cvt_pk_f32_fp8_sdwa v[118:119], v42 src0_sel:WORD_1
	v_cvt_pk_f32_fp8_e32 v[120:121], v43
	v_cvt_pk_f32_fp8_sdwa v[122:123], v43 src0_sel:WORD_1
	v_cvt_pk_f32_fp8_e32 v[124:125], v64
	v_cvt_pk_f32_fp8_sdwa v[126:127], v64 src0_sel:WORD_1
	v_cvt_pk_f32_fp8_e32 v[128:129], v65
	v_cvt_pk_f32_fp8_sdwa v[130:131], v65 src0_sel:WORD_1
	v_pk_mul_f32 v[92:93], v[116:117], v[124:125]
	v_pk_mul_f32 v[94:95], v[118:119], v[126:127]
	v_pk_mul_f32 v[96:97], v[120:121], v[128:129]
	v_pk_mul_f32 v[98:99], v[122:123], v[130:131]
	s_add_u32 s16, s12, 4
	s_cmp_ge_u32 s16, s13
	s_cbranch_scc1 .Lcv_piece_done
	s_movk_i32 s17, 0xff
	s_cmp_lt_u32 s16, 0x4000
	s_cselect_b32 s17, 0xfff, s17
	s_and_b32 s18, s16, s17
	s_cmp_eq_u32 s18, 0
	s_cbranch_scc1 .Lcv_nohp_4
	v_pk_mul_f32 v[132:133], v[6:7], v[100:101]
	v_pk_mul_f32 v[134:135], v[8:9], v[102:103]
	v_pk_mul_f32 v[136:137], v[10:11], v[104:105]
	v_pk_mul_f32 v[138:139], v[12:13], v[106:107]
	s_branch .Lcv_hp_4

.Lcv_nohn_4:
	v_cvt_pk_f32_fp8_e32 v[116:117], v82
	v_cvt_pk_f32_fp8_sdwa v[118:119], v82 src0_sel:WORD_1
	v_cvt_pk_f32_fp8_e32 v[120:121], v83
	v_cvt_pk_f32_fp8_sdwa v[122:123], v83 src0_sel:WORD_1
	v_pk_mul_f32 v[116:117], v[116:117], 0.5 op_sel_hi:[1,0]
	v_pk_mul_f32 v[118:119], v[118:119], 0.5 op_sel_hi:[1,0]
	v_pk_mul_f32 v[120:121], v[120:121], 0.5 op_sel_hi:[1,0]
	v_pk_mul_f32 v[122:123], v[122:123], 0.5 op_sel_hi:[1,0]
	v_pk_mul_f32 v[132:133], v[116:117], v[132:133]
	v_pk_mul_f32 v[134:135], v[118:119], v[134:135]
	v_pk_mul_f32 v[136:137], v[120:121], v[136:137]
	v_pk_mul_f32 v[138:139], v[122:123], v[138:139]
	v_med3_f32 v132, v132, s79, v204
	v_med3_f32 v133, v133, s79, v204
	v_med3_f32 v134, v134, s79, v204
	v_med3_f32 v135, v135, s79, v204
	v_med3_f32 v136, v136, s79, v204
	v_med3_f32 v137, v137, s79, v204
	v_med3_f32 v138, v138, s79, v204
	v_med3_f32 v139, v139, s79, v204
	v_mov_b32_e32 v124, 0
	v_mov_b32_e32 v125, 0
	v_cvt_pk_fp8_f32 v124, v132, v133
	v_cvt_pk_fp8_f32 v125, v136, v137
	v_cvt_pk_fp8_f32 v124, v134, v135 op_sel:[0,0,1]
	v_cvt_pk_fp8_f32 v125, v138, v139 op_sel:[0,0,1]
	s_lshl_b32 s17, s16, 12
	s_add_u32 s52, s40, s17
	s_addc_u32 s53, s41, 0
	global_store_dwordx2 v140, v[124:125], s[52:53]
	v_cvt_pk_f32_fp8_e32 v[116:117], v44
	v_cvt_pk_f32_fp8_sdwa v[118:119], v44 src0_sel:WORD_1
	v_cvt_pk_f32_fp8_e32 v[120:121], v45
	v_cvt_pk_f32_fp8_sdwa v[122:123], v45 src0_sel:WORD_1
	v_cvt_pk_f32_fp8_e32 v[124:125], v66
	v_cvt_pk_f32_fp8_sdwa v[126:127], v66 src0_sel:WORD_1
	v_cvt_pk_f32_fp8_e32 v[128:129], v67
	v_cvt_pk_f32_fp8_sdwa v[130:131], v67 src0_sel:WORD_1
	v_pk_mul_f32 v[100:101], v[116:117], v[124:125]
	v_pk_mul_f32 v[102:103], v[118:119], v[126:127]
	v_pk_mul_f32 v[104:105], v[120:121], v[128:129]
	v_pk_mul_f32 v[106:107], v[122:123], v[130:131]
	s_add_u32 s16, s12, 5
	s_cmp_ge_u32 s16, s13
	s_cbranch_scc1 .Lcv_piece_done
	s_movk_i32 s17, 0xff
	s_cmp_lt_u32 s16, 0x4000
	s_cselect_b32 s17, 0xfff, s17
	s_and_b32 s18, s16, s17
	s_cmp_eq_u32 s18, 0
	s_cbranch_scc1 .Lcv_nohp_5
	v_pk_mul_f32 v[132:133], v[6:7], v[108:109]
	v_pk_mul_f32 v[134:135], v[8:9], v[110:111]
	v_pk_mul_f32 v[136:137], v[10:11], v[112:113]
	v_pk_mul_f32 v[138:139], v[12:13], v[114:115]
	s_branch .Lcv_hp_5

.Lcv_nohn_5:
	v_cvt_pk_f32_fp8_e32 v[116:117], v84
	v_cvt_pk_f32_fp8_sdwa v[118:119], v84 src0_sel:WORD_1
	v_cvt_pk_f32_fp8_e32 v[120:121], v85
	v_cvt_pk_f32_fp8_sdwa v[122:123], v85 src0_sel:WORD_1
	v_pk_mul_f32 v[116:117], v[116:117], 0.5 op_sel_hi:[1,0]
	v_pk_mul_f32 v[118:119], v[118:119], 0.5 op_sel_hi:[1,0]
	v_pk_mul_f32 v[120:121], v[120:121], 0.5 op_sel_hi:[1,0]
	v_pk_mul_f32 v[122:123], v[122:123], 0.5 op_sel_hi:[1,0]
	v_pk_mul_f32 v[132:133], v[116:117], v[132:133]
	v_pk_mul_f32 v[134:135], v[118:119], v[134:135]
	v_pk_mul_f32 v[136:137], v[120:121], v[136:137]
	v_pk_mul_f32 v[138:139], v[122:123], v[138:139]
	v_med3_f32 v132, v132, s79, v204
	v_med3_f32 v133, v133, s79, v204
	v_med3_f32 v134, v134, s79, v204
	v_med3_f32 v135, v135, s79, v204
	v_med3_f32 v136, v136, s79, v204
	v_med3_f32 v137, v137, s79, v204
	v_med3_f32 v138, v138, s79, v204
	v_med3_f32 v139, v139, s79, v204
	v_mov_b32_e32 v124, 0
	v_mov_b32_e32 v125, 0
	v_cvt_pk_fp8_f32 v124, v132, v133
	v_cvt_pk_fp8_f32 v125, v136, v137
	v_cvt_pk_fp8_f32 v124, v134, v135 op_sel:[0,0,1]
	v_cvt_pk_fp8_f32 v125, v138, v139 op_sel:[0,0,1]
	s_lshl_b32 s17, s16, 12
	s_add_u32 s52, s40, s17
	s_addc_u32 s53, s41, 0
	global_store_dwordx2 v140, v[124:125], s[52:53]
	v_cvt_pk_f32_fp8_e32 v[116:117], v46
	v_cvt_pk_f32_fp8_sdwa v[118:119], v46 src0_sel:WORD_1
	v_cvt_pk_f32_fp8_e32 v[120:121], v47
	v_cvt_pk_f32_fp8_sdwa v[122:123], v47 src0_sel:WORD_1
	v_cvt_pk_f32_fp8_e32 v[124:125], v68
	v_cvt_pk_f32_fp8_sdwa v[126:127], v68 src0_sel:WORD_1
	v_cvt_pk_f32_fp8_e32 v[128:129], v69
	v_cvt_pk_f32_fp8_sdwa v[130:131], v69 src0_sel:WORD_1
	v_pk_mul_f32 v[108:109], v[116:117], v[124:125]
	v_pk_mul_f32 v[110:111], v[118:119], v[126:127]
	v_pk_mul_f32 v[112:113], v[120:121], v[128:129]
	v_pk_mul_f32 v[114:115], v[122:123], v[130:131]
	s_add_u32 s16, s12, 6
	s_cmp_ge_u32 s16, s13
	s_cbranch_scc1 .Lcv_piece_done
	s_movk_i32 s17, 0xff
	s_cmp_lt_u32 s16, 0x4000
	s_cselect_b32 s17, 0xfff, s17
	s_and_b32 s18, s16, s17
	s_cmp_eq_u32 s18, 0
	s_cbranch_scc1 .Lcv_nohp_6
	v_pk_mul_f32 v[132:133], v[6:7], v[92:93]
	v_pk_mul_f32 v[134:135], v[8:9], v[94:95]
	v_pk_mul_f32 v[136:137], v[10:11], v[96:97]
	v_pk_mul_f32 v[138:139], v[12:13], v[98:99]
	s_branch .Lcv_hp_6

.Lcv_nohn_6:
	v_cvt_pk_f32_fp8_e32 v[116:117], v86
	v_cvt_pk_f32_fp8_sdwa v[118:119], v86 src0_sel:WORD_1
	v_cvt_pk_f32_fp8_e32 v[120:121], v87
	v_cvt_pk_f32_fp8_sdwa v[122:123], v87 src0_sel:WORD_1
	v_pk_mul_f32 v[116:117], v[116:117], 0.5 op_sel_hi:[1,0]
	v_pk_mul_f32 v[118:119], v[118:119], 0.5 op_sel_hi:[1,0]
	v_pk_mul_f32 v[120:121], v[120:121], 0.5 op_sel_hi:[1,0]
	v_pk_mul_f32 v[122:123], v[122:123], 0.5 op_sel_hi:[1,0]
	v_pk_mul_f32 v[132:133], v[116:117], v[132:133]
	v_pk_mul_f32 v[134:135], v[118:119], v[134:135]
	v_pk_mul_f32 v[136:137], v[120:121], v[136:137]
	v_pk_mul_f32 v[138:139], v[122:123], v[138:139]
	v_med3_f32 v132, v132, s79, v204
	v_med3_f32 v133, v133, s79, v204
	v_med3_f32 v134, v134, s79, v204
	v_med3_f32 v135, v135, s79, v204
	v_med3_f32 v136, v136, s79, v204
	v_med3_f32 v137, v137, s79, v204
	v_med3_f32 v138, v138, s79, v204
	v_med3_f32 v139, v139, s79, v204
	v_mov_b32_e32 v124, 0
	v_mov_b32_e32 v125, 0
	v_cvt_pk_fp8_f32 v124, v132, v133
	v_cvt_pk_fp8_f32 v125, v136, v137
	v_cvt_pk_fp8_f32 v124, v134, v135 op_sel:[0,0,1]
	v_cvt_pk_fp8_f32 v125, v138, v139 op_sel:[0,0,1]
	s_lshl_b32 s17, s16, 12
	s_add_u32 s52, s40, s17
	s_addc_u32 s53, s41, 0
	global_store_dwordx2 v140, v[124:125], s[52:53]
	v_cvt_pk_f32_fp8_e32 v[116:117], v48
	v_cvt_pk_f32_fp8_sdwa v[118:119], v48 src0_sel:WORD_1
	v_cvt_pk_f32_fp8_e32 v[120:121], v49
	v_cvt_pk_f32_fp8_sdwa v[122:123], v49 src0_sel:WORD_1
	v_cvt_pk_f32_fp8_e32 v[124:125], v70
	v_cvt_pk_f32_fp8_sdwa v[126:127], v70 src0_sel:WORD_1
	v_cvt_pk_f32_fp8_e32 v[128:129], v71
	v_cvt_pk_f32_fp8_sdwa v[130:131], v71 src0_sel:WORD_1
	v_pk_mul_f32 v[92:93], v[116:117], v[124:125]
	v_pk_mul_f32 v[94:95], v[118:119], v[126:127]
	v_pk_mul_f32 v[96:97], v[120:121], v[128:129]
	v_pk_mul_f32 v[98:99], v[122:123], v[130:131]
	s_add_u32 s16, s12, 7
	s_cmp_ge_u32 s16, s13
	s_cbranch_scc1 .Lcv_piece_done
	s_movk_i32 s17, 0xff
	s_cmp_lt_u32 s16, 0x4000
	s_cselect_b32 s17, 0xfff, s17
	s_and_b32 s18, s16, s17
	s_cmp_eq_u32 s18, 0
	s_cbranch_scc1 .Lcv_nohp_7
	v_pk_mul_f32 v[132:133], v[6:7], v[100:101]
	v_pk_mul_f32 v[134:135], v[8:9], v[102:103]
	v_pk_mul_f32 v[136:137], v[10:11], v[104:105]
	v_pk_mul_f32 v[138:139], v[12:13], v[106:107]
	s_branch .Lcv_hp_7

.Lcv_nohn_7:
	v_cvt_pk_f32_fp8_e32 v[116:117], v88
	v_cvt_pk_f32_fp8_sdwa v[118:119], v88 src0_sel:WORD_1
	v_cvt_pk_f32_fp8_e32 v[120:121], v89
	v_cvt_pk_f32_fp8_sdwa v[122:123], v89 src0_sel:WORD_1
	v_pk_mul_f32 v[116:117], v[116:117], 0.5 op_sel_hi:[1,0]
	v_pk_mul_f32 v[118:119], v[118:119], 0.5 op_sel_hi:[1,0]
	v_pk_mul_f32 v[120:121], v[120:121], 0.5 op_sel_hi:[1,0]
	v_pk_mul_f32 v[122:123], v[122:123], 0.5 op_sel_hi:[1,0]
	v_pk_mul_f32 v[132:133], v[116:117], v[132:133]
	v_pk_mul_f32 v[134:135], v[118:119], v[134:135]
	v_pk_mul_f32 v[136:137], v[120:121], v[136:137]
	v_pk_mul_f32 v[138:139], v[122:123], v[138:139]
	v_med3_f32 v132, v132, s79, v204
	v_med3_f32 v133, v133, s79, v204
	v_med3_f32 v134, v134, s79, v204
	v_med3_f32 v135, v135, s79, v204
	v_med3_f32 v136, v136, s79, v204
	v_med3_f32 v137, v137, s79, v204
	v_med3_f32 v138, v138, s79, v204
	v_med3_f32 v139, v139, s79, v204
	v_mov_b32_e32 v124, 0
	v_mov_b32_e32 v125, 0
	v_cvt_pk_fp8_f32 v124, v132, v133
	v_cvt_pk_fp8_f32 v125, v136, v137
	v_cvt_pk_fp8_f32 v124, v134, v135 op_sel:[0,0,1]
	v_cvt_pk_fp8_f32 v125, v138, v139 op_sel:[0,0,1]
	s_lshl_b32 s17, s16, 12
	s_add_u32 s52, s40, s17
	s_addc_u32 s53, s41, 0
	global_store_dwordx2 v140, v[124:125], s[52:53]
	v_cvt_pk_f32_fp8_e32 v[116:117], v50
	v_cvt_pk_f32_fp8_sdwa v[118:119], v50 src0_sel:WORD_1
	v_cvt_pk_f32_fp8_e32 v[120:121], v51
	v_cvt_pk_f32_fp8_sdwa v[122:123], v51 src0_sel:WORD_1
	v_cvt_pk_f32_fp8_e32 v[124:125], v72
	v_cvt_pk_f32_fp8_sdwa v[126:127], v72 src0_sel:WORD_1
	v_cvt_pk_f32_fp8_e32 v[128:129], v73
	v_cvt_pk_f32_fp8_sdwa v[130:131], v73 src0_sel:WORD_1
	v_pk_mul_f32 v[100:101], v[116:117], v[124:125]
	v_pk_mul_f32 v[102:103], v[118:119], v[126:127]
	v_pk_mul_f32 v[104:105], v[120:121], v[128:129]
	v_pk_mul_f32 v[106:107], v[122:123], v[130:131]
	s_add_u32 s16, s12, 8
	s_cmp_ge_u32 s16, s13
	s_cbranch_scc1 .Lcv_piece_done
	s_movk_i32 s17, 0xff
	s_cmp_lt_u32 s16, 0x4000
	s_cselect_b32 s17, 0xfff, s17
	s_and_b32 s18, s16, s17
	s_cmp_eq_u32 s18, 0
	s_cbranch_scc1 .Lcv_nohp_8
	v_pk_mul_f32 v[132:133], v[6:7], v[108:109]
	v_pk_mul_f32 v[134:135], v[8:9], v[110:111]
	v_pk_mul_f32 v[136:137], v[10:11], v[112:113]
	v_pk_mul_f32 v[138:139], v[12:13], v[114:115]
	s_branch .Lcv_hp_8

.Lcv_nohn_8:
	v_cvt_pk_f32_fp8_e32 v[116:117], v90
	v_cvt_pk_f32_fp8_sdwa v[118:119], v90 src0_sel:WORD_1
	v_cvt_pk_f32_fp8_e32 v[120:121], v91
	v_cvt_pk_f32_fp8_sdwa v[122:123], v91 src0_sel:WORD_1
	v_pk_mul_f32 v[116:117], v[116:117], 0.5 op_sel_hi:[1,0]
	v_pk_mul_f32 v[118:119], v[118:119], 0.5 op_sel_hi:[1,0]
	v_pk_mul_f32 v[120:121], v[120:121], 0.5 op_sel_hi:[1,0]
	v_pk_mul_f32 v[122:123], v[122:123], 0.5 op_sel_hi:[1,0]
	v_pk_mul_f32 v[132:133], v[116:117], v[132:133]
	v_pk_mul_f32 v[134:135], v[118:119], v[134:135]
	v_pk_mul_f32 v[136:137], v[120:121], v[136:137]
	v_pk_mul_f32 v[138:139], v[122:123], v[138:139]
	v_med3_f32 v132, v132, s79, v204
	v_med3_f32 v133, v133, s79, v204
	v_med3_f32 v134, v134, s79, v204
	v_med3_f32 v135, v135, s79, v204
	v_med3_f32 v136, v136, s79, v204
	v_med3_f32 v137, v137, s79, v204
	v_med3_f32 v138, v138, s79, v204
	v_med3_f32 v139, v139, s79, v204
	v_mov_b32_e32 v124, 0
	v_mov_b32_e32 v125, 0
	v_cvt_pk_fp8_f32 v124, v132, v133
	v_cvt_pk_fp8_f32 v125, v136, v137
	v_cvt_pk_fp8_f32 v124, v134, v135 op_sel:[0,0,1]
	v_cvt_pk_fp8_f32 v125, v138, v139 op_sel:[0,0,1]
	s_lshl_b32 s17, s16, 12
	s_add_u32 s52, s40, s17
	s_addc_u32 s53, s41, 0
	global_store_dwordx2 v140, v[124:125], s[52:53]
.Lcv_piece_done:
	s_add_u32 s42, s42, 1
	s_cmp_lt_u32 s42, 4
	s_cbranch_scc1 .Lcv_piece
	s_add_u32 s12, s12, 9
	s_cmp_lt_u32 s12, s13
	s_cbranch_scc1 .Lcv_chunk
.Lcv_end:
.LBB0_414:
	s_cmpk_gt_i32 s6, 0x10f
	s_cbranch_scc1 .LBB0_449
	s_waitcnt vmcnt(0)
	v_bfe_u32 v9, v5, 8, 1
	v_and_b32_e32 v6, 0x7f, v5
	v_bfe_u32 v8, v5, 7, 1
	v_lshlrev_b32_e32 v7, 11, v9
	v_readlane_b32 s8, v254, 0
	v_lshlrev_b32_e32 v9, 1, v9
	s_waitcnt lgkmcnt(0)
	v_bfe_u32 v10, v5, 2, 2
	v_lshl_or_b32 v16, v8, 14, v7
	v_add_u32_e32 v13, 0, v6
	v_lshlrev_b32_e32 v6, 6, v6
	v_mov_b32_e32 v7, v4
	v_readlane_b32 s9, v254, 1
	v_bitop3_b32 v8, v9, v10, v8 bitop3:0x36
	v_lshlrev_b32_e32 v8, 4, v8
	v_lshl_add_u64 v[6:7], s[8:9], 0, v[6:7]
	v_mov_b32_e32 v9, v4
	v_lshl_add_u64 v[6:7], v[6:7], 0, v[8:9]
	v_add_u32_e32 v8, 0x600, v5
	v_readlane_b32 s8, v252, 43
	v_mov_b32_e32 v3, v4
	v_ashrrev_i32_e32 v14, 9, v8
	v_ashrrev_i32_e32 v8, 9, v5
	v_add_u32_e32 v10, 0x200, v5
	v_add_u32_e32 v5, 0x400, v5
	v_readlane_b32 s9, v252, 44
	s_lshl_b32 s7, s5, 3
	v_add_u32_e32 v18, 0, v2
	v_ashrrev_i32_e32 v10, 9, v10
	v_ashrrev_i32_e32 v12, 9, v5
	v_lshl_add_u64 v[2:3], s[8:9], 0, v[2:3]
	s_lshl_b32 s8, s6, 6
	v_lshl_add_u32 v17, v14, 7, v13
	s_lshl_b32 s5, s5, 12
	v_lshl_add_u32 v19, v8, 7, v13
	v_ashrrev_i32_e32 v9, 31, v8
	v_lshl_add_u32 v20, v10, 7, v13
	v_ashrrev_i32_e32 v11, 31, v10
	v_lshl_add_u32 v21, v12, 7, v13
	v_ashrrev_i32_e32 v13, 31, v12
	v_ashrrev_i32_e32 v15, 31, v14
	s_add_i32 s8, s8, s7
	s_or_b32 s14, s5, 0x200
	s_or_b32 s15, s5, 0x400
	s_or_b32 s16, s5, 0x600
	s_or_b32 s17, s5, 0x800
	s_or_b32 s18, s5, 0xa00
	s_or_b32 s19, s5, 0xc00
	s_or_b32 s38, s5, 0xe00
	v_lshlrev_b64 v[8:9], 13, v[8:9]
	v_lshlrev_b64 v[10:11], 13, v[10:11]
	v_lshlrev_b64 v[12:13], 13, v[12:13]
	v_lshlrev_b64 v[14:15], 13, v[14:15]
	s_or_b32 s39, s8, 7
	v_add_u32_e32 v5, v19, v16
	v_add_u32_e32 v19, v20, v16
	v_add_u32_e32 v20, v21, v16
	v_add_u32_e32 v21, v17, v16
	s_branch .LBB0_417
